# speedup vs baseline: 1.0103x; 1.0049x over previous
.Lmy_back_4:
	ds_read_b64_tr_b16 v[54:55], v181 offset:49152
	ds_read_b64_tr_b16 v[56:57], v181 offset:49664
	v_add_f32_e32 v49, v80, v81
	v_cvt_pk_f16_f32 v50, v80, v81
	v_cvt_pk_f16_f32 v51, v82, v83
	v_cvt_pk_f16_f32 v52, v84, v85
	v_cvt_pk_f16_f32 v53, v86, v87
	ds_read_b64_tr_b16 v[58:59], v181 offset:50176
	ds_read_b64_tr_b16 v[60:61], v181 offset:50688
	s_waitcnt lgkmcnt(2)
	v_mfma_f32_32x32x16_f16 v[16:31], v[50:53], v[54:57], v[16:31]
	ds_read_b64_tr_b16 v[54:55], v181 offset:53248
	ds_read_b64_tr_b16 v[56:57], v181 offset:53760
	v_add_f32_e32 v49, v82, v49
	v_add_f32_e32 v49, v83, v49
	v_add_f32_e32 v49, v84, v49
	v_add_f32_e32 v49, v85, v49
	v_add_f32_e32 v49, v86, v49
	v_add_f32_e32 v49, v87, v49
	s_waitcnt lgkmcnt(0)
	v_mfma_f32_32x32x16_f16 v[32:47], v[50:53], v[54:57], v[32:47]
	v_add_f32_e32 v49, v88, v49
	v_add_f32_e32 v49, v89, v49
	ds_read_b64_tr_b16 v[62:63], v181 offset:54272
	ds_read_b64_tr_b16 v[64:65], v181 offset:54784
	v_add_f32_e32 v49, v90, v49
	v_add_f32_e32 v49, v91, v49
	v_cvt_pk_f16_f32 v50, v88, v89
	v_cvt_pk_f16_f32 v51, v90, v91
	v_cvt_pk_f16_f32 v52, v92, v93
	v_cvt_pk_f16_f32 v53, v94, v95
	v_add_f32_e32 v49, v92, v49
	v_mfma_f32_32x32x16_f16 v[16:31], v[50:53], v[58:61], v[16:31]
	v_add_f32_e32 v49, v93, v49
	v_add_f32_e32 v49, v94, v49
	v_add_f32_e32 v49, v95, v49
	v_add_f32_e32 v49, v0, v49
	v_add_f32_e32 v49, v1, v49
	v_add_f32_e32 v49, v2, v49
	v_add_f32_e32 v49, v3, v49
	s_waitcnt lgkmcnt(0)
	v_mfma_f32_32x32x16_f16 v[32:47], v[50:53], v[62:65], v[32:47]
	ds_read_b64_tr_b16 v[50:51], v181 offset:51200
	ds_read_b64_tr_b16 v[52:53], v181 offset:51712
	v_cvt_pk_f16_f32 v0, v0, v1
	v_cvt_pk_f16_f32 v1, v2, v3
	v_cvt_pk_f16_f32 v2, v4, v5
	v_cvt_pk_f16_f32 v3, v6, v7
	ds_read_b64_tr_b16 v[54:55], v181 offset:52224
	ds_read_b64_tr_b16 v[56:57], v181 offset:52736
	v_add_f32_e32 v4, v4, v49
	s_waitcnt lgkmcnt(2)
	v_mfma_f32_32x32x16_f16 v[16:31], v[0:3], v[50:53], v[16:31]
	ds_read_b64_tr_b16 v[50:51], v181 offset:55296
	ds_read_b64_tr_b16 v[52:53], v181 offset:55808
	v_add_f32_e32 v4, v5, v4
	v_add_f32_e32 v4, v6, v4
	ds_read_b64_tr_b16 v[58:59], v181 offset:56320
	ds_read_b64_tr_b16 v[60:61], v181 offset:56832
	v_cvt_pk_f16_f32 v5, v14, v15
	s_waitcnt lgkmcnt(2)
	v_mfma_f32_32x32x16_f16 v[32:47], v[0:3], v[50:53], v[32:47]
	v_add_f32_e32 v0, v7, v4
	v_add_f32_e32 v0, v8, v0
	v_add_f32_e32 v0, v9, v0
	v_add_f32_e32 v0, v10, v0
	v_cvt_pk_f16_f32 v2, v8, v9
	v_cvt_pk_f16_f32 v3, v10, v11
	v_cvt_pk_f16_f32 v4, v12, v13
	v_add_f32_e32 v0, v11, v0
	v_mfma_f32_32x32x16_f16 v[16:31], v[2:5], v[54:57], v[16:31]
	v_add_f32_e32 v0, v12, v0
	v_add_f32_e32 v0, v13, v0
	v_add_f32_e32 v0, v14, v0
	v_add_f32_e32 v0, v15, v0
	v_add_f32_e32 v0, v176, v0
	v_mov_b32_e32 v1, v0
	s_nop 1
	v_permlane32_swap_b32_e32 v0, v1
	s_waitcnt lgkmcnt(0)
	v_mfma_f32_32x32x16_f16 v[32:47], v[2:5], v[58:61], v[32:47]
	s_and_saveexec_b64 s[2:3], s[0:1]
	v_add_f32_e32 v0, v0, v1
	ds_write_b32 v186, v0 offset:57472
	s_or_b64 exec, exec, s[2:3]
	s_waitcnt lgkmcnt(0)
	ds_read_b128 v[0:3], v48 offset:57472
	ds_read_b128 v[4:7], v48 offset:57504
	s_mov_b32 s11, 0
	s_lshl_b64 s[0:1], s[10:11], 22
	s_add_u32 s0, s8, s0
	s_waitcnt lgkmcnt(1)
	v_rcp_f32_e32 v8, v0
	v_rcp_f32_e32 v9, v1
	s_addc_u32 s1, s9, s1
	s_lshl_b32 s2, s23, 12
	v_rcp_f32_e32 v10, v2
	v_rcp_f32_e32 v11, v3
	s_waitcnt lgkmcnt(0)
	v_rcp_f32_e32 v12, v4
	ds_read_b128 v[0:3], v48 offset:57536
	v_rcp_f32_e32 v13, v5
	v_rcp_f32_e32 v14, v6
	v_rcp_f32_e32 v15, v7
	ds_read_b128 v[4:7], v48 offset:57568
	s_add_i32 s6, s2, 0
	v_lshlrev_b32_e32 v48, 1, v189
	v_add3_u32 v48, s6, v191, v48
	v_fma_mixlo_f16 v16, v16, v8, 0
	v_fma_mixlo_f16 v8, v32, v8, 0
	ds_write_b16 v48, v8 offset:59456
	v_fma_mixlo_f16 v8, v17, v9, 0
	ds_write_b16 v48, v8 offset:59520
	v_fma_mixlo_f16 v8, v33, v9, 0
	ds_write_b16 v48, v8 offset:59584
	v_fma_mixlo_f16 v8, v18, v10, 0
	ds_write_b16 v48, v8 offset:59648
	v_fma_mixlo_f16 v8, v34, v10, 0
	ds_write_b16 v48, v8 offset:59712
	v_fma_mixlo_f16 v8, v19, v11, 0
	ds_write_b16 v48, v8 offset:59776
	v_fma_mixlo_f16 v8, v35, v11, 0
	ds_write_b16 v48, v8 offset:59840
	v_fma_mixlo_f16 v8, v20, v12, 0
	ds_write_b16 v48, v8 offset:60416
	v_fma_mixlo_f16 v8, v36, v12, 0
	ds_write_b16 v48, v8 offset:60480
	v_fma_mixlo_f16 v8, v21, v13, 0
	ds_write_b16 v48, v8 offset:60544
	v_fma_mixlo_f16 v8, v37, v13, 0
	s_waitcnt lgkmcnt(11)
	v_rcp_f32_e32 v0, v0
	ds_write_b16 v48, v8 offset:60608
	v_fma_mixlo_f16 v8, v22, v14, 0
	v_rcp_f32_e32 v1, v1
	ds_write_b16 v48, v8 offset:60672
	v_fma_mixlo_f16 v8, v38, v14, 0
	ds_write_b16 v48, v8 offset:60736
	v_fma_mixlo_f16 v8, v23, v15, 0
	v_rcp_f32_e32 v2, v2
	ds_write_b16 v48, v8 offset:60800
	v_fma_mixlo_f16 v8, v39, v15, 0
	ds_write_b16 v48, v8 offset:60864
	v_fma_mixlo_f16 v8, v24, v0, 0
	v_fma_mixlo_f16 v0, v40, v0, 0
	v_rcp_f32_e32 v3, v3
	ds_write_b16 v48, v0 offset:61504
	v_fma_mixlo_f16 v0, v25, v1, 0
	ds_write_b16 v48, v0 offset:61568
	v_fma_mixlo_f16 v0, v41, v1, 0
	s_waitcnt lgkmcnt(14)
	v_rcp_f32_e32 v4, v4
	ds_write_b16 v48, v0 offset:61632
	v_fma_mixlo_f16 v0, v26, v2, 0
	ds_write_b16 v48, v0 offset:61696
	v_fma_mixlo_f16 v0, v42, v2, 0
	v_rcp_f32_e32 v5, v5
	ds_write_b16 v48, v0 offset:61760
	v_fma_mixlo_f16 v0, v27, v3, 0
	ds_write_b16 v48, v0 offset:61824
	v_fma_mixlo_f16 v0, v43, v3, 0
	v_rcp_f32_e32 v6, v6
	ds_write_b16 v48, v0 offset:61888
	v_fma_mixlo_f16 v0, v28, v4, 0
	ds_write_b16 v48, v0 offset:62464
	v_fma_mixlo_f16 v0, v44, v4, 0
	v_rcp_f32_e32 v7, v7
	ds_write_b16 v48, v0 offset:62528
	v_fma_mixlo_f16 v0, v29, v5, 0
	ds_write_b16 v48, v0 offset:62592
	v_fma_mixlo_f16 v0, v45, v5, 0
	ds_write_b16 v48, v0 offset:62656
	v_fma_mixlo_f16 v0, v30, v6, 0
	ds_write_b16 v48, v0 offset:62720
	v_fma_mixlo_f16 v0, v46, v6, 0
	ds_write_b16 v48, v0 offset:62784
	v_fma_mixlo_f16 v0, v31, v7, 0
	ds_write_b16 v48, v0 offset:62848
	v_fma_mixlo_f16 v0, v47, v7, 0
	ds_write_b16 v48, v0 offset:62912
	v_lshrrev_b32_e32 v0, 3, v188
	v_and_b32_e32 v4, 56, v190
	s_lshl_b32 s4, s24, 8
	s_lshl_b32 s5, s22, 9
	ds_write_b16 v48, v16 offset:59392
	ds_write_b16 v48, v8 offset:61440
	v_lshlrev_b32_e32 v1, 7, v0
	v_lshlrev_b32_e32 v2, 1, v4
	s_waitcnt lgkmcnt(0)
	v_add3_u32 v8, s6, v1, v2
	s_or_b32 s4, s4, s5
	v_or_b32_e32 v5, s4, v0
	ds_read_b128 v[0:3], v8 offset:59392
	ds_read_b128 v[16:19], v8 offset:60416
	ds_read_b128 v[20:23], v8 offset:61440
	ds_read_b128 v[24:27], v8 offset:62464
	s_lshl_b32 s7, s20, 6
	v_add_lshl_u32 v5, v5, s21, 8
	v_or3_b32 v4, v5, s7, v4
	s_and_b32 s1, s1, 0xffff
	s_mov_b32 s3, 0x20000
	s_mov_b32 s2, 0x400000
	v_lshlrev_b32_e32 v12, 1, v4
	v_add_u32_e32 v13, 0x1000, v12
	v_add_u32_e32 v14, 0x2000, v12
	v_add_u32_e32 v15, 0x3000, v12
	s_waitcnt lgkmcnt(3)
	buffer_store_dwordx4 v[0:3], v12, s[0:3], 0 offen sc1
	s_waitcnt lgkmcnt(2)
	buffer_store_dwordx4 v[16:19], v13, s[0:3], 0 offen sc1
	s_waitcnt lgkmcnt(1)
	buffer_store_dwordx4 v[20:23], v14, s[0:3], 0 offen sc1
	s_waitcnt lgkmcnt(0)
	buffer_store_dwordx4 v[24:27], v15, s[0:3], 0 offen sc1
	s_endpgm
